# pipelined attention + barrier placed 3 fragments early: last MFMAs of a block run after the barrier while the next block's LDS reads are in flight
# speedup vs baseline: 1.0016x; 1.0016x over previous
.LBB0_733:
	s_or_b64 exec, exec, s[8:9]
	s_movk_i32 s4, 0xf0
	s_cmp_lg_u32 0, -1
	v_lshlrev_b32_e32 v39, 8, v141
	v_bitop3_b32 v80, v142, s4, v136 bitop3:0x48
	s_cselect_b32 s10, 0, 0
	v_cvt_pk_bf16_f32 v96, v134, v135
	v_cvt_pk_bf16_f32 v97, v132, v133
	v_cvt_pk_bf16_f32 v98, v130, v131
	v_cvt_pk_bf16_f32 v99, v128, v129
	v_cvt_pk_bf16_f32 v100, v126, v127
	v_cvt_pk_bf16_f32 v101, v124, v125
	v_cvt_pk_bf16_f32 v102, v122, v123
	v_cvt_pk_bf16_f32 v103, v120, v121
	v_cvt_pk_bf16_f32 v104, v70, v71
	v_cvt_pk_bf16_f32 v105, v74, v75
	v_cvt_pk_bf16_f32 v106, v64, v65
	v_cvt_pk_bf16_f32 v107, v68, v69
	v_cvt_pk_bf16_f32 v108, v60, v61
	v_cvt_pk_bf16_f32 v109, v66, v67
	v_cvt_pk_bf16_f32 v110, v56, v57
	v_cvt_pk_bf16_f32 v111, v58, v59
	v_cvt_pk_bf16_f32 v112, v112, v113
	v_cvt_pk_bf16_f32 v113, v118, v119
	v_cvt_pk_bf16_f32 v114, v114, v115
	v_cvt_pk_bf16_f32 v115, v116, v117
	v_cvt_pk_bf16_f32 v116, v78, v79
	v_cvt_pk_bf16_f32 v117, v76, v77
	v_cvt_pk_bf16_f32 v118, v72, v73
	v_cvt_pk_bf16_f32 v119, v62, v63
	v_cvt_pk_bf16_f32 v120, v52, v53
	v_cvt_pk_bf16_f32 v121, v54, v55
	v_cvt_pk_bf16_f32 v122, v46, v47
	v_cvt_pk_bf16_f32 v123, v50, v51
	v_cvt_pk_bf16_f32 v124, v44, v45
	v_cvt_pk_bf16_f32 v125, v48, v49
	v_cvt_pk_bf16_f32 v126, v40, v41
	v_cvt_pk_bf16_f32 v127, v42, v43
	v_readlane_b32 s100, v250, 8
	v_mbcnt_lo_u32_b32 v68, -1, 0
	v_mbcnt_hi_u32_b32 v68, -1, v68
	s_nop 1
	v_add_u32_e32 v69, s100, v68
	v_lshrrev_b32_e32 v70, 3, v69
	v_and_b32_e32 v71, 7, v69
	v_lshrrev_b32_e32 v72, 2, v71
	v_bfe_u32 v73, v71, 1, 1
	v_and_b32_e32 v74, 1, v71
	v_lshlrev_b32_e32 v74, 1, v74
	v_lshl_add_u32 v75, v72, 2, v74
	v_bfe_u32 v76, v70, 1, 3
	v_xor_b32_e32 v77, v75, v76
	v_add_u32_e32 v78, 1, v75
	v_xor_b32_e32 v78, v78, v76
	v_lshlrev_b32_e32 v79, 7, v70
	v_lshl_add_u32 v79, v73, 3, v79
	v_lshl_add_u32 v64, v77, 4, v79
	v_lshl_add_u32 v65, v78, 4, v79
	v_add_u32_e32 v66, 0x2000, v64
	v_add_u32_e32 v67, 0x2000, v65
	v_or_b32_e32 v81, v39, v80
	s_add_i32 s15, s10, 0x10000
	v_and_b32_e32 v82, 6, v137
	v_lshrrev_b32_e32 v84, 4, v136
	s_waitcnt vmcnt(0)
	s_waitcnt vmcnt(0)
	s_add_i32 s11, s10, 0x12000
	v_lshl_add_u32 v83, v139, 7, s10
	v_bitop3_b32 v85, v84, v82, 7 bitop3:0x6c
	v_and_b32_e32 v86, 8, v138
	v_or_b32_e32 v82, 1, v82
	v_add_u32_e32 v225, s15, v81
	s_waitcnt vmcnt(4)
	ds_write_b128 v225, v[24:27] offset:0
	v_lshlrev_b32_e32 v85, 4, v85
	v_add_u32_e32 v87, v83, v86
	v_bitop3_b32 v82, v84, v82, 7 bitop3:0x6c
	v_add3_u32 v226, v80, s11, v39
	ds_write_b128 v226, v[28:31] offset:0
	v_lshlrev_b32_e32 v82, 4, v82
	v_add_u32_e32 v227, v87, v85
	ds_write_b64 v64, v[12:13] offset:0
	v_lshrrev_b32_e32 v32, 5, v136
	v_add_u32_e32 v83, 0x2000, v83
	v_or_b32_e32 v84, v85, v86
	v_add_u32_e32 v228, v87, v82
	ds_write_b64 v65, v[14:15] offset:0
	v_xor_b32_e32 v32, v32, v137
	v_or_b32_e32 v86, v82, v86
	v_add_u32_e32 v229, v84, v83
	ds_write_b64 v66, v[4:5] offset:0
	v_lshlrev_b32_e32 v32, 4, v32
	v_add_u32_e32 v184, v86, v83
	ds_write_b64 v67, v[6:7] offset:0
	v_lshlrev_b32_e32 v33, 8, v143
	v_and_b32_e32 v32, 16, v32
	v_bfe_u32 v35, v137, 1, 3
	s_waitcnt vmcnt(4)
	ds_write_b128 v225, v[20:23] offset:0x4000
	v_lshlrev_b32_e32 v36, 5, v35
	v_add3_u32 v32, v33, s15, v32
	s_movk_i32 s16, 0x60
	ds_write_b128 v226, v[16:19] offset:0x4000
	v_xad_u32 v204, v36, s16, v32
	s_movk_i32 s16, 0x80
	ds_write_b64 v64, v[8:9] offset:0x4000
	v_xad_u32 v205, v36, s16, v32
	s_movk_i32 s16, 0xa0
	ds_write_b64 v65, v[10:11] offset:0x4000
	s_add_u32 s8, s6, 0x100
	v_xad_u32 v206, v36, s16, v32
	s_movk_i32 s16, 0xc0
	ds_write_b64 v66, v[0:1] offset:0x4000
	s_addc_u32 s9, s7, 0
	v_xad_u32 v207, v36, s16, v32
	s_movk_i32 s16, 0xe0
	ds_write_b64 v67, v[2:3] offset:0x4000
	v_add_u32_e32 v201, v32, v36
	v_xad_u32 v202, v36, 32, v32
	v_xad_u32 v203, v36, 64, v32
	v_xad_u32 v208, v36, s16, v32
	v_lshl_add_u32 v32, v143, 7, s10
	s_add_u32 s10, s78, 0x20000
	global_load_dwordx4 v[132:135], v198, s[8:9]
	s_addc_u32 s11, s79, 0
	global_load_dwordx4 v[128:131], v199, s[8:9]
	v_lshrrev_b32_e32 v34, 1, v137
	global_load_dwordx4 v[136:139], v196, s[10:11]
	s_add_u32 s6, s6, 0x180
	v_bitop3_b32 v34, v140, v34, 7 bitop3:0x78
	v_bitop3_b32 v37, v140, v35, 2 bitop3:0x36
	v_bitop3_b32 v38, v140, v35, 4 bitop3:0x36
	v_bitop3_b32 v35, v140, v35, 6 bitop3:0x36
	global_load_dwordx4 v[140:143], v197, s[10:11]
	s_addc_u32 s7, s7, 0
	s_add_u32 s8, s78, 0x30000
	global_load_dwordx4 v[148:151], v198, s[6:7]
	s_addc_u32 s9, s79, 0
	global_load_dwordx4 v[144:147], v199, s[6:7]
	global_load_dwordx4 v[152:155], v196, s[8:9]
	s_add_u32 s10, s13, s14
	global_load_dwordx4 v[156:159], v197, s[8:9]
	s_addc_u32 s11, s12, 0
	s_add_u32 s12, s41, s30
	v_mov_b32_e32 v0, 0
	s_mov_b32 s4, 0
	v_lshl_add_u32 v209, v34, 4, v32
	v_lshl_add_u32 v210, v37, 4, v32
	v_lshl_add_u32 v211, v38, 4, v32
	v_lshl_add_u32 v224, v35, 4, v32
	s_addc_u32 s13, 0, s31
	v_mov_b32_e32 v1, v0
	v_mov_b32_e32 v2, v0
	v_mov_b32_e32 v3, v0
	v_mov_b32_e32 v4, v0
	v_mov_b32_e32 v5, v0
	v_mov_b32_e32 v6, v0
	v_mov_b32_e32 v7, v0
	v_mov_b32_e32 v8, v0
	v_mov_b32_e32 v9, v0
	v_mov_b32_e32 v10, v0
	v_mov_b32_e32 v11, v0
	v_mov_b32_e32 v12, v0
	v_mov_b32_e32 v13, v0
	v_mov_b32_e32 v14, v0
	v_mov_b32_e32 v15, v0
	v_mov_b32_e32 v16, v0
	v_mov_b32_e32 v17, v0
	v_mov_b32_e32 v18, v0
	v_mov_b32_e32 v19, v0
	v_mov_b32_e32 v20, v0
	v_mov_b32_e32 v21, v0
	v_mov_b32_e32 v22, v0
	v_mov_b32_e32 v23, v0
	v_mov_b32_e32 v24, v0
	v_mov_b32_e32 v25, v0
	v_mov_b32_e32 v26, v0
	v_mov_b32_e32 v27, v0
	v_mov_b32_e32 v28, v0
	v_mov_b32_e32 v29, v0
	v_mov_b32_e32 v30, v0
	v_mov_b32_e32 v31, v0
	v_mov_b32_e32 v32, v0
	v_mov_b32_e32 v33, v0
	v_mov_b32_e32 v34, v0
	v_mov_b32_e32 v35, v0
	v_mov_b32_e32 v36, v0
	v_mov_b32_e32 v37, v0
	v_mov_b32_e32 v38, v0
	v_mov_b32_e32 v39, v0
	v_mov_b32_e32 v40, v0
	v_mov_b32_e32 v41, v0
	v_mov_b32_e32 v42, v0
	v_mov_b32_e32 v43, v0
	v_mov_b32_e32 v44, v0
	v_mov_b32_e32 v45, v0
	v_mov_b32_e32 v46, v0
	v_mov_b32_e32 v47, v0
	v_mov_b32_e32 v48, v0
	v_mov_b32_e32 v49, v0
	v_mov_b32_e32 v50, v0
	v_mov_b32_e32 v51, v0
	v_mov_b32_e32 v52, v0
	v_mov_b32_e32 v53, v0
	v_mov_b32_e32 v54, v0
	v_mov_b32_e32 v55, v0
	v_mov_b32_e32 v56, v0
	v_mov_b32_e32 v57, v0
	v_mov_b32_e32 v58, v0
	v_mov_b32_e32 v59, v0
	v_mov_b32_e32 v60, v0
	v_mov_b32_e32 v61, v0
	v_mov_b32_e32 v62, v0
	v_mov_b32_e32 v63, v0
	v_mov_b32_e32 v160, v0
	v_mov_b32_e32 v161, v0
	v_mov_b32_e32 v227, v64
	v_mov_b32_e32 v228, v65
	v_mov_b32_e32 v229, v66
	v_mov_b32_e32 v184, v67
	v_readlane_b32 s100, v250, 8
	v_mbcnt_lo_u32_b32 v68, -1, 0
	v_mbcnt_hi_u32_b32 v68, -1, v68
	v_and_b32_e32 v69, 15, v68
	v_lshrrev_b32_e32 v70, 4, v68
	v_lshlrev_b32_e32 v72, 8, v69
	v_add_u32_e32 v72, 0x10000, v72
	v_add_u32_e32 v71, 0, v70
	v_xor_b32_e32 v71, v71, v69
	v_lshl_add_u32 v201, v71, 4, v72
	v_add_u32_e32 v71, 4, v70
	v_xor_b32_e32 v71, v71, v69
	v_lshl_add_u32 v202, v71, 4, v72
	v_add_u32_e32 v71, 8, v70
	v_xor_b32_e32 v71, v71, v69
	v_lshl_add_u32 v203, v71, 4, v72
	v_add_u32_e32 v71, 12, v70
	v_xor_b32_e32 v71, v71, v69
	v_lshl_add_u32 v246, v71, 4, v72
	v_bfe_u32 v73, v69, 1, 3
	v_lshlrev_b32_e32 v76, 7, v69
	v_add_u32_e32 v71, 0, v70
	v_xor_b32_e32 v71, v71, v73
	v_lshl_add_u32 v209, v71, 4, v76
	v_add_u32_e32 v71, 4, v70
	v_xor_b32_e32 v71, v71, v73
	v_lshl_add_u32 v210, v71, 4, v76
	s_lshl_b32 s101, s100, 7
	s_add_u32 s101, s101, 0x8000
	s_cmpk_ge_u32 s100, 0x100
	s_cselect_b32 s6, 0x8000, 0
	s_add_u32 s101, s101, s6
	v_and_b32_e32 v74, 31, v68
	v_lshrrev_b32_e32 v75, 5, v68
	v_lshlrev_b32_e32 v74, 8, v74
	v_lshl_add_u32 v74, v75, 4, v74
	v_add_u32_e32 v74, s101, v74
	v_lshlrev_b32_e32 v75, 8, v69
	v_lshl_add_u32 v75, v70, 4, v75
	v_add_u32_e32 v75, s101, v75
	ds_write_b128 v74, v[96:99] offset:0
	ds_write_b128 v74, v[100:103] offset:32
	ds_write_b128 v74, v[104:107] offset:64
	ds_write_b128 v74, v[108:111] offset:96
	ds_write_b128 v74, v[112:115] offset:128
	ds_write_b128 v74, v[116:119] offset:160
	ds_write_b128 v74, v[120:123] offset:192
	ds_write_b128 v74, v[124:127] offset:224
	s_waitcnt lgkmcnt(0)
	ds_read_b128 v[96:99], v75 offset:0
	ds_read_b128 v[100:103], v75 offset:64
	ds_read_b128 v[104:107], v75 offset:128
	ds_read_b128 v[108:111], v75 offset:192
	ds_read_b128 v[112:115], v75 offset:4096
	ds_read_b128 v[116:119], v75 offset:4160
	ds_read_b128 v[120:123], v75 offset:4224
	ds_read_b128 v[124:127], v75 offset:4288
	s_waitcnt vmcnt(0)
	s_waitcnt lgkmcnt(0)
	s_barrier
	ds_write_b128 v225, v[136:139] offset:32768
	ds_write_b128 v226, v[140:143] offset:32768
	s_add_u32 s15, s22, s12
	s_addc_u32 s14, s23, s13
	s_add_u32 s6, s15, 0x23a40000
	s_addc_u32 s7, s14, 0
	s_waitcnt lgkmcnt(0)
	global_load_dwordx4 v[136:139], v196, s[6:7]
	global_load_dwordx4 v[140:143], v197, s[6:7]
	v_mov_b32_e32 v194, 0
	v_mov_b32_e32 v195, 0
	s_barrier
	ds_read_b128 v[160:163], v201 offset:0
	ds_read_b128 v[164:167], v202 offset:0
	ds_read_b128 v[168:171], v203 offset:0
	ds_read_b128 v[172:175], v246 offset:0
	ds_read_b128 v[176:179], v201 offset:4096
	ds_read_b128 v[180:183], v202 offset:4096
	ds_read_b128 v[230:233], v203 offset:4096
	s_waitcnt lgkmcnt(6)
	v_mfma_f32_16x16x32_bf16 v[64:67], v[160:163], v[96:99], 0
	v_mfma_f32_16x16x32_bf16 v[68:71], v[160:163], v[112:115], 0
	ds_read_b128 v[234:237], v246 offset:4096
	s_waitcnt lgkmcnt(6)
	v_mfma_f32_16x16x32_bf16 v[68:71], v[164:167], v[116:119], v[68:71]
	v_mfma_f32_16x16x32_bf16 v[64:67], v[164:167], v[100:103], v[64:67]
	ds_read_b128 v[160:163], v201 offset:8192
	s_waitcnt lgkmcnt(6)
	v_mfma_f32_16x16x32_bf16 v[64:67], v[168:171], v[104:107], v[64:67]
	v_mfma_f32_16x16x32_bf16 v[68:71], v[168:171], v[120:123], v[68:71]
	ds_read_b128 v[164:167], v202 offset:8192
	s_waitcnt lgkmcnt(6)
	v_mfma_f32_16x16x32_bf16 v[68:71], v[172:175], v[124:127], v[68:71]
	v_mfma_f32_16x16x32_bf16 v[64:67], v[172:175], v[108:111], v[64:67]
	ds_read_b128 v[168:171], v203 offset:8192
	s_waitcnt lgkmcnt(6)
	v_mfma_f32_16x16x32_bf16 v[72:75], v[176:179], v[96:99], 0
	s_nop 7
	s_nop 1
	v_exp_f32_e32 v64, v64
	v_exp_f32_e32 v68, v68
	v_mfma_f32_16x16x32_bf16 v[76:79], v[176:179], v[112:115], 0
	v_exp_f32_e32 v65, v65
	v_exp_f32_e32 v69, v69
	ds_read_b128 v[172:175], v246 offset:8192
	s_waitcnt lgkmcnt(6)
	v_mfma_f32_16x16x32_bf16 v[76:79], v[180:183], v[116:119], v[76:79]
	v_exp_f32_e32 v66, v66
	v_exp_f32_e32 v70, v70
	v_mfma_f32_16x16x32_bf16 v[72:75], v[180:183], v[100:103], v[72:75]
	v_exp_f32_e32 v67, v67
	v_exp_f32_e32 v71, v71
	ds_read_b128 v[176:179], v201 offset:12288
	s_waitcnt lgkmcnt(6)
	v_mfma_f32_16x16x32_bf16 v[72:75], v[230:233], v[104:107], v[72:75]
	v_add_f32_e32 v220, v64, v65
	v_add_f32_e32 v221, v68, v69
	v_mfma_f32_16x16x32_bf16 v[76:79], v[230:233], v[120:123], v[76:79]
	v_add_f32_e32 v220, v220, v66
	v_add_f32_e32 v221, v221, v70
	ds_read_b128 v[180:183], v202 offset:12288
	s_waitcnt lgkmcnt(6)
	v_mfma_f32_16x16x32_bf16 v[76:79], v[234:237], v[124:127], v[76:79]
	v_add_f32_e32 v220, v220, v67
	v_mfma_f32_16x16x32_bf16 v[72:75], v[234:237], v[108:111], v[72:75]
	v_add_f32_e32 v221, v221, v71
	ds_read_b128 v[230:233], v203 offset:12288
	s_waitcnt lgkmcnt(6)
	v_mfma_f32_16x16x32_bf16 v[80:83], v[160:163], v[96:99], 0
	s_nop 7
	s_nop 1
	v_exp_f32_e32 v72, v72
	v_exp_f32_e32 v76, v76
	v_exp_f32_e32 v73, v73
	v_mfma_f32_16x16x32_bf16 v[84:87], v[160:163], v[112:115], 0
	v_exp_f32_e32 v77, v77
	v_exp_f32_e32 v74, v74
	v_exp_f32_e32 v78, v78
	ds_read_b128 v[234:237], v246 offset:12288
	s_waitcnt lgkmcnt(6)
	v_mfma_f32_16x16x32_bf16 v[84:87], v[164:167], v[116:119], v[84:87]
	v_exp_f32_e32 v75, v75
	v_exp_f32_e32 v79, v79
	v_add_f32_e32 v220, v220, v72
	v_mfma_f32_16x16x32_bf16 v[80:83], v[164:167], v[100:103], v[80:83]
	v_add_f32_e32 v221, v221, v76
	v_add_f32_e32 v220, v220, v73
	v_add_f32_e32 v221, v221, v77
	s_waitcnt lgkmcnt(5)
	v_mfma_f32_16x16x32_bf16 v[80:83], v[168:171], v[104:107], v[80:83]
	v_add_f32_e32 v220, v220, v74
	v_add_f32_e32 v221, v221, v78
	v_add_f32_e32 v220, v220, v75
	v_mfma_f32_16x16x32_bf16 v[84:87], v[168:171], v[120:123], v[84:87]
	v_add_f32_e32 v221, v221, v79
	v_cvt_pk_bf16_f32 v216, v64, v65
	v_cvt_pk_bf16_f32 v217, v66, v67
	s_waitcnt lgkmcnt(4)
	v_mfma_f32_16x16x32_bf16 v[84:87], v[172:175], v[124:127], v[84:87]
	v_cvt_pk_bf16_f32 v238, v68, v69
	v_cvt_pk_bf16_f32 v239, v70, v71
	v_cvt_pk_bf16_f32 v218, v72, v73
	v_mfma_f32_16x16x32_bf16 v[80:83], v[172:175], v[108:111], v[80:83]
	v_cvt_pk_bf16_f32 v219, v74, v75
	v_cvt_pk_bf16_f32 v240, v76, v77
	v_cvt_pk_bf16_f32 v241, v78, v79
	s_waitcnt lgkmcnt(3)
	v_mfma_f32_16x16x32_bf16 v[88:91], v[176:179], v[96:99], 0
	s_nop 7
	s_nop 1
	v_exp_f32_e32 v80, v80
	v_exp_f32_e32 v84, v84
	v_mfma_f32_16x16x32_bf16 v[92:95], v[176:179], v[112:115], 0
	v_exp_f32_e32 v81, v81
	v_exp_f32_e32 v85, v85
	s_waitcnt lgkmcnt(2)
	v_mfma_f32_16x16x32_bf16 v[92:95], v[180:183], v[116:119], v[92:95]
	v_exp_f32_e32 v82, v82
	v_exp_f32_e32 v86, v86
	v_mfma_f32_16x16x32_bf16 v[88:91], v[180:183], v[100:103], v[88:91]
	v_exp_f32_e32 v83, v83
	v_exp_f32_e32 v87, v87
	s_waitcnt lgkmcnt(1)
	v_mfma_f32_16x16x32_bf16 v[88:91], v[230:233], v[104:107], v[88:91]
	v_add_f32_e32 v220, v220, v80
	v_add_f32_e32 v221, v221, v84
	v_mfma_f32_16x16x32_bf16 v[92:95], v[230:233], v[120:123], v[92:95]
	v_add_f32_e32 v220, v220, v81
	v_add_f32_e32 v221, v221, v85
	s_waitcnt lgkmcnt(0)
	v_mfma_f32_16x16x32_bf16 v[92:95], v[234:237], v[124:127], v[92:95]
	v_add_f32_e32 v220, v220, v82
	v_add_f32_e32 v221, v221, v86
	v_mfma_f32_16x16x32_bf16 v[88:91], v[234:237], v[108:111], v[88:91]
	v_add_f32_e32 v220, v220, v83
	v_add_f32_e32 v221, v221, v87
	s_waitcnt lgkmcnt(0)
	s_barrier
	ds_read_b128 v[160:163], v201 offset:16384
	ds_read_b128 v[164:167], v209 offset:0
	ds_read_b128 v[168:171], v202 offset:16384
	ds_read_b128 v[172:175], v209 offset:2048
	ds_read_b128 v[176:179], v203 offset:16384
	ds_read_b128 v[180:183], v209 offset:4096
	ds_read_b128 v[230:233], v246 offset:16384
.LBB0_734:
	s_waitcnt lgkmcnt(6)
	v_mfma_f32_16x16x32_bf16 v[64:67], v[160:163], v[96:99], 0
	v_exp_f32_e32 v88, v88
	v_exp_f32_e32 v92, v92
	v_mfma_f32_16x16x32_bf16 v[68:71], v[160:163], v[112:115], 0
	v_cvt_pk_bf16_f32 v242, v80, v81
	v_exp_f32_e32 v89, v89
	ds_read_b128 v[234:237], v209 offset:6144
	s_add_u32 s16, s22, s10
	s_addc_u32 s17, s23, s11
	s_add_u32 s15, s22, s12
	s_addc_u32 s14, s23, s13
	s_add_u32 s8, s16, 0x3bc00200
	s_addc_u32 s9, s17, 0
	s_add_u32 s6, s15, 0x23a50000
	s_addc_u32 s7, s14, 0
	s_waitcnt lgkmcnt(6)
	v_mfma_f32_16x16x32_bf16 v[0:3], v[164:167], v[216:219], v[0:3]
	v_exp_f32_e32 v93, v93
	v_cvt_pk_bf16_f32 v243, v82, v83
	v_mfma_f32_16x16x32_bf16 v[4:7], v[164:167], v[238:241], v[4:7]
	v_exp_f32_e32 v90, v90
	v_exp_f32_e32 v94, v94
	ds_read_b128 v[160:163], v201 offset:20480
	s_waitcnt vmcnt(4)
	ds_write_b128 v225, v[152:155] offset:49152
	s_waitcnt lgkmcnt(7)
	v_mfma_f32_16x16x32_bf16 v[68:71], v[168:171], v[116:119], v[68:71]
	v_cvt_pk_bf16_f32 v204, v84, v85
	v_mfma_f32_16x16x32_bf16 v[64:67], v[168:171], v[100:103], v[64:67]
	v_exp_f32_e32 v91, v91
	ds_read_b128 v[164:167], v209 offset:8192
	ds_write_b128 v226, v[156:159] offset:49152
	s_waitcnt lgkmcnt(8)
	v_mfma_f32_16x16x32_bf16 v[12:15], v[172:175], v[238:241], v[12:15]
	v_exp_f32_e32 v95, v95
	v_mfma_f32_16x16x32_bf16 v[8:11], v[172:175], v[216:219], v[8:11]
	v_cvt_pk_bf16_f32 v205, v86, v87
	ds_read_b128 v[168:171], v202 offset:20480
	ds_write_b64 v227, v[132:133] offset:32768
	s_waitcnt lgkmcnt(9)
	v_mfma_f32_16x16x32_bf16 v[64:67], v[176:179], v[104:107], v[64:67]
	v_add_f32_e32 v220, v220, v88
	v_mfma_f32_16x16x32_bf16 v[68:71], v[176:179], v[120:123], v[68:71]
	v_add_f32_e32 v221, v221, v92
	ds_read_b128 v[172:175], v209 offset:10240
	ds_write_b64 v228, v[134:135] offset:32768
	s_waitcnt lgkmcnt(10)
	v_mfma_f32_16x16x32_bf16 v[16:19], v[180:183], v[216:219], v[16:19]
	v_add_f32_e32 v220, v220, v89
	v_mfma_f32_16x16x32_bf16 v[20:23], v[180:183], v[238:241], v[20:23]
	v_add_f32_e32 v221, v221, v93
	ds_read_b128 v[176:179], v203 offset:20480
	ds_write_b64 v229, v[128:129] offset:32768
	s_waitcnt lgkmcnt(11)
	v_mfma_f32_16x16x32_bf16 v[68:71], v[230:233], v[124:127], v[68:71]
	v_cvt_pk_bf16_f32 v244, v88, v89
	v_mfma_f32_16x16x32_bf16 v[64:67], v[230:233], v[108:111], v[64:67]
	v_cvt_pk_bf16_f32 v245, v90, v91
	ds_read_b128 v[180:183], v209 offset:12288
	ds_write_b64 v184, v[130:131] offset:32768
	s_waitcnt lgkmcnt(12)
	v_mfma_f32_16x16x32_bf16 v[28:31], v[234:237], v[238:241], v[28:31]
	v_cvt_pk_bf16_f32 v206, v92, v93
	v_mfma_f32_16x16x32_bf16 v[24:27], v[234:237], v[216:219], v[24:27]
	v_cvt_pk_bf16_f32 v207, v94, v95
	ds_read_b128 v[230:233], v246 offset:20480
	global_load_dwordx4 v[132:135], v198, s[8:9]
	s_waitcnt lgkmcnt(12)
	v_mfma_f32_16x16x32_bf16 v[72:75], v[160:163], v[96:99], 0
	v_add_f32_e32 v220, v220, v90
	v_add_f32_e32 v221, v221, v94
	v_mfma_f32_16x16x32_bf16 v[76:79], v[160:163], v[112:115], 0
	v_add_f32_e32 v220, v220, v91
	v_add_f32_e32 v221, v221, v95
	ds_read_b128 v[234:237], v209 offset:14336
	global_load_dwordx4 v[128:131], v199, s[8:9]
	s_waitcnt lgkmcnt(11)
	v_mfma_f32_16x16x32_bf16 v[32:35], v[164:167], v[216:219], v[32:35]
	v_add_f32_e32 v194, v194, v220
	v_add_f32_e32 v195, v195, v221
	v_mfma_f32_16x16x32_bf16 v[36:39], v[164:167], v[238:241], v[36:39]
	v_exp_f32_e32 v64, v64
	v_exp_f32_e32 v68, v68
	ds_read_b128 v[160:163], v201 offset:24576
	global_load_dwordx4 v[152:155], v196, s[6:7]
	s_waitcnt lgkmcnt(10)
	v_mfma_f32_16x16x32_bf16 v[76:79], v[168:171], v[116:119], v[76:79]
	v_exp_f32_e32 v65, v65
	v_mfma_f32_16x16x32_bf16 v[72:75], v[168:171], v[100:103], v[72:75]
	v_exp_f32_e32 v69, v69
	ds_read_b128 v[164:167], v210 offset:0
	global_load_dwordx4 v[156:159], v197, s[6:7]
	s_waitcnt lgkmcnt(9)
	v_mfma_f32_16x16x32_bf16 v[44:47], v[172:175], v[238:241], v[44:47]
	v_exp_f32_e32 v66, v66
	v_mfma_f32_16x16x32_bf16 v[40:43], v[172:175], v[216:219], v[40:43]
	v_exp_f32_e32 v70, v70
	ds_read_b128 v[168:171], v202 offset:24576
	s_waitcnt lgkmcnt(8)
	v_mfma_f32_16x16x32_bf16 v[72:75], v[176:179], v[104:107], v[72:75]
	v_exp_f32_e32 v67, v67
	v_mfma_f32_16x16x32_bf16 v[76:79], v[176:179], v[120:123], v[76:79]
	v_exp_f32_e32 v71, v71
	ds_read_b128 v[172:175], v210 offset:2048
	s_waitcnt lgkmcnt(7)
	v_mfma_f32_16x16x32_bf16 v[48:51], v[180:183], v[216:219], v[48:51]
	v_add_f32_e32 v220, v64, v65
	v_mfma_f32_16x16x32_bf16 v[52:55], v[180:183], v[238:241], v[52:55]
	v_add_f32_e32 v221, v68, v69
	ds_read_b128 v[176:179], v203 offset:24576
	s_waitcnt lgkmcnt(6)
	v_mfma_f32_16x16x32_bf16 v[76:79], v[230:233], v[124:127], v[76:79]
	v_add_f32_e32 v220, v220, v66
	v_mfma_f32_16x16x32_bf16 v[72:75], v[230:233], v[108:111], v[72:75]
	v_add_f32_e32 v221, v221, v70
	ds_read_b128 v[180:183], v210 offset:4096
	s_waitcnt lgkmcnt(6)
	v_mfma_f32_16x16x32_bf16 v[60:63], v[234:237], v[238:241], v[60:63]
	v_add_f32_e32 v220, v220, v67
	v_mfma_f32_16x16x32_bf16 v[56:59], v[234:237], v[216:219], v[56:59]
	v_add_f32_e32 v221, v221, v71
	ds_read_b128 v[230:233], v246 offset:24576
	s_waitcnt lgkmcnt(6)
	v_mfma_f32_16x16x32_bf16 v[80:83], v[160:163], v[96:99], 0
	v_exp_f32_e32 v72, v72
	v_exp_f32_e32 v76, v76
	v_mfma_f32_16x16x32_bf16 v[84:87], v[160:163], v[112:115], 0
	v_exp_f32_e32 v73, v73
	v_exp_f32_e32 v77, v77
	ds_read_b128 v[234:237], v210 offset:6144
	s_waitcnt lgkmcnt(6)
	v_mfma_f32_16x16x32_bf16 v[0:3], v[164:167], v[242:245], v[0:3]
	v_exp_f32_e32 v74, v74
	v_exp_f32_e32 v78, v78
	v_mfma_f32_16x16x32_bf16 v[4:7], v[164:167], v[204:207], v[4:7]
	v_exp_f32_e32 v75, v75
	v_exp_f32_e32 v79, v79
	ds_read_b128 v[160:163], v201 offset:28672
	s_waitcnt lgkmcnt(6)
	v_mfma_f32_16x16x32_bf16 v[84:87], v[168:171], v[116:119], v[84:87]
	v_add_f32_e32 v220, v220, v72
	v_mfma_f32_16x16x32_bf16 v[80:83], v[168:171], v[100:103], v[80:83]
	v_add_f32_e32 v221, v221, v76
	ds_read_b128 v[164:167], v210 offset:8192
	s_waitcnt lgkmcnt(6)
	v_mfma_f32_16x16x32_bf16 v[12:15], v[172:175], v[204:207], v[12:15]
	v_add_f32_e32 v220, v220, v73
	v_mfma_f32_16x16x32_bf16 v[8:11], v[172:175], v[242:245], v[8:11]
	v_add_f32_e32 v221, v221, v77
	ds_read_b128 v[168:171], v202 offset:28672
	s_waitcnt lgkmcnt(6)
	v_mfma_f32_16x16x32_bf16 v[80:83], v[176:179], v[104:107], v[80:83]
	v_add_f32_e32 v220, v220, v74
	v_mfma_f32_16x16x32_bf16 v[84:87], v[176:179], v[120:123], v[84:87]
	v_add_f32_e32 v221, v221, v78
	ds_read_b128 v[172:175], v210 offset:10240
	s_waitcnt lgkmcnt(6)
	v_mfma_f32_16x16x32_bf16 v[16:19], v[180:183], v[242:245], v[16:19]
	v_add_f32_e32 v220, v220, v75
	v_mfma_f32_16x16x32_bf16 v[20:23], v[180:183], v[204:207], v[20:23]
	v_add_f32_e32 v221, v221, v79
	ds_read_b128 v[176:179], v203 offset:28672
	s_waitcnt lgkmcnt(6)
	v_mfma_f32_16x16x32_bf16 v[84:87], v[230:233], v[124:127], v[84:87]
	v_cvt_pk_bf16_f32 v216, v64, v65
	v_mfma_f32_16x16x32_bf16 v[80:83], v[230:233], v[108:111], v[80:83]
	v_cvt_pk_bf16_f32 v217, v66, v67
	ds_read_b128 v[180:183], v210 offset:12288
	s_waitcnt lgkmcnt(6)
	v_mfma_f32_16x16x32_bf16 v[28:31], v[234:237], v[204:207], v[28:31]
	v_cvt_pk_bf16_f32 v238, v68, v69
	v_mfma_f32_16x16x32_bf16 v[24:27], v[234:237], v[242:245], v[24:27]
	v_cvt_pk_bf16_f32 v239, v70, v71
	ds_read_b128 v[230:233], v246 offset:28672
	s_waitcnt lgkmcnt(6)
	v_mfma_f32_16x16x32_bf16 v[88:91], v[160:163], v[96:99], 0
	v_exp_f32_e32 v80, v80
	v_exp_f32_e32 v84, v84
	v_mfma_f32_16x16x32_bf16 v[92:95], v[160:163], v[112:115], 0
	v_exp_f32_e32 v81, v81
	v_exp_f32_e32 v85, v85
	ds_read_b128 v[234:237], v210 offset:14336
	s_waitcnt lgkmcnt(6)
	v_mfma_f32_16x16x32_bf16 v[32:35], v[164:167], v[242:245], v[32:35]
	v_exp_f32_e32 v82, v82
	v_exp_f32_e32 v86, v86
	v_mfma_f32_16x16x32_bf16 v[36:39], v[164:167], v[204:207], v[36:39]
	v_exp_f32_e32 v83, v83
	v_exp_f32_e32 v87, v87
	ds_read_b128 v[160:163], v201 offset:32768
	s_waitcnt lgkmcnt(6)
	v_mfma_f32_16x16x32_bf16 v[92:95], v[168:171], v[116:119], v[92:95]
	v_add_f32_e32 v220, v220, v80
	v_mfma_f32_16x16x32_bf16 v[88:91], v[168:171], v[100:103], v[88:91]
	v_add_f32_e32 v221, v221, v84
	ds_read_b128 v[164:167], v209 offset:16384
	s_waitcnt lgkmcnt(6)
	v_mfma_f32_16x16x32_bf16 v[44:47], v[172:175], v[204:207], v[44:47]
	v_add_f32_e32 v220, v220, v81
	v_mfma_f32_16x16x32_bf16 v[40:43], v[172:175], v[242:245], v[40:43]
	v_add_f32_e32 v221, v221, v85
	ds_read_b128 v[168:171], v202 offset:32768
	s_waitcnt lgkmcnt(6)
	v_mfma_f32_16x16x32_bf16 v[88:91], v[176:179], v[104:107], v[88:91]
	v_add_f32_e32 v220, v220, v82
	v_mfma_f32_16x16x32_bf16 v[92:95], v[176:179], v[120:123], v[92:95]
	v_add_f32_e32 v221, v221, v86
	ds_read_b128 v[172:175], v209 offset:18432
	s_waitcnt lgkmcnt(6)
	v_mfma_f32_16x16x32_bf16 v[48:51], v[180:183], v[242:245], v[48:51]
	v_add_f32_e32 v220, v220, v83
	v_mfma_f32_16x16x32_bf16 v[52:55], v[180:183], v[204:207], v[52:55]
	v_add_f32_e32 v221, v221, v87
	ds_read_b128 v[176:179], v203 offset:32768
	s_waitcnt lgkmcnt(6)
	v_mfma_f32_16x16x32_bf16 v[92:95], v[230:233], v[124:127], v[92:95]
	v_cvt_pk_bf16_f32 v218, v72, v73
	v_mfma_f32_16x16x32_bf16 v[88:91], v[230:233], v[108:111], v[88:91]
	v_cvt_pk_bf16_f32 v219, v74, v75
	ds_read_b128 v[180:183], v209 offset:20480
	s_waitcnt lgkmcnt(6)
	v_mfma_f32_16x16x32_bf16 v[60:63], v[234:237], v[204:207], v[60:63]
	v_cvt_pk_bf16_f32 v240, v76, v77
	v_mfma_f32_16x16x32_bf16 v[56:59], v[234:237], v[242:245], v[56:59]
	v_cvt_pk_bf16_f32 v241, v78, v79
	ds_read_b128 v[230:233], v246 offset:32768
	s_waitcnt lgkmcnt(6)
	v_mfma_f32_16x16x32_bf16 v[64:67], v[160:163], v[96:99], 0
	v_exp_f32_e32 v88, v88
	v_exp_f32_e32 v92, v92
	v_mfma_f32_16x16x32_bf16 v[68:71], v[160:163], v[112:115], 0
	v_cvt_pk_bf16_f32 v242, v80, v81
	v_exp_f32_e32 v89, v89
	ds_read_b128 v[234:237], v209 offset:22528
	s_add_u32 s8, s16, 0x3bc00280
	s_addc_u32 s9, s17, 0
	s_add_u32 s6, s15, 0x23a60000
	s_addc_u32 s7, s14, 0
	s_waitcnt lgkmcnt(6)
	v_mfma_f32_16x16x32_bf16 v[0:3], v[164:167], v[216:219], v[0:3]
	v_exp_f32_e32 v93, v93
	v_cvt_pk_bf16_f32 v243, v82, v83
	v_mfma_f32_16x16x32_bf16 v[4:7], v[164:167], v[238:241], v[4:7]
	v_exp_f32_e32 v90, v90
	v_exp_f32_e32 v94, v94
	ds_read_b128 v[160:163], v201 offset:36864
	s_waitcnt vmcnt(4)
	ds_write_b128 v225, v[136:139] offset:0
	s_waitcnt lgkmcnt(7)
	v_mfma_f32_16x16x32_bf16 v[68:71], v[168:171], v[116:119], v[68:71]
	v_cvt_pk_bf16_f32 v204, v84, v85
	v_mfma_f32_16x16x32_bf16 v[64:67], v[168:171], v[100:103], v[64:67]
	v_exp_f32_e32 v91, v91
	ds_read_b128 v[164:167], v209 offset:24576
	ds_write_b128 v226, v[140:143] offset:0
	s_waitcnt lgkmcnt(8)
	v_mfma_f32_16x16x32_bf16 v[12:15], v[172:175], v[238:241], v[12:15]
	v_exp_f32_e32 v95, v95
	v_mfma_f32_16x16x32_bf16 v[8:11], v[172:175], v[216:219], v[8:11]
	v_cvt_pk_bf16_f32 v205, v86, v87
	ds_read_b128 v[168:171], v202 offset:36864
	ds_write_b64 v227, v[148:149] offset:49152
	s_waitcnt lgkmcnt(9)
	v_mfma_f32_16x16x32_bf16 v[64:67], v[176:179], v[104:107], v[64:67]
	v_add_f32_e32 v220, v220, v88
	v_mfma_f32_16x16x32_bf16 v[68:71], v[176:179], v[120:123], v[68:71]
	v_add_f32_e32 v221, v221, v92
	ds_read_b128 v[172:175], v209 offset:26624
	ds_write_b64 v228, v[150:151] offset:49152
	s_waitcnt lgkmcnt(10)
	v_mfma_f32_16x16x32_bf16 v[16:19], v[180:183], v[216:219], v[16:19]
	v_add_f32_e32 v220, v220, v89
	v_mfma_f32_16x16x32_bf16 v[20:23], v[180:183], v[238:241], v[20:23]
	v_add_f32_e32 v221, v221, v93
	ds_read_b128 v[176:179], v203 offset:36864
	ds_write_b64 v229, v[144:145] offset:49152
	s_waitcnt lgkmcnt(11)
	v_mfma_f32_16x16x32_bf16 v[68:71], v[230:233], v[124:127], v[68:71]
	v_cvt_pk_bf16_f32 v244, v88, v89
	v_mfma_f32_16x16x32_bf16 v[64:67], v[230:233], v[108:111], v[64:67]
	v_cvt_pk_bf16_f32 v245, v90, v91
	ds_read_b128 v[180:183], v209 offset:28672
	ds_write_b64 v184, v[146:147] offset:49152
	s_waitcnt lgkmcnt(12)
	v_mfma_f32_16x16x32_bf16 v[28:31], v[234:237], v[238:241], v[28:31]
	v_cvt_pk_bf16_f32 v206, v92, v93
	v_mfma_f32_16x16x32_bf16 v[24:27], v[234:237], v[216:219], v[24:27]
	v_cvt_pk_bf16_f32 v207, v94, v95
	ds_read_b128 v[230:233], v246 offset:36864
	global_load_dwordx4 v[148:151], v198, s[8:9]
	s_waitcnt lgkmcnt(12)
	v_mfma_f32_16x16x32_bf16 v[72:75], v[160:163], v[96:99], 0
	v_add_f32_e32 v220, v220, v90
	v_add_f32_e32 v221, v221, v94
	v_mfma_f32_16x16x32_bf16 v[76:79], v[160:163], v[112:115], 0
	v_add_f32_e32 v220, v220, v91
	v_add_f32_e32 v221, v221, v95
	ds_read_b128 v[234:237], v209 offset:30720
	global_load_dwordx4 v[144:147], v199, s[8:9]
	s_waitcnt lgkmcnt(11)
	v_mfma_f32_16x16x32_bf16 v[32:35], v[164:167], v[216:219], v[32:35]
	v_add_f32_e32 v194, v194, v220
	v_add_f32_e32 v195, v195, v221
	v_mfma_f32_16x16x32_bf16 v[36:39], v[164:167], v[238:241], v[36:39]
	v_exp_f32_e32 v64, v64
	v_exp_f32_e32 v68, v68
	ds_read_b128 v[160:163], v201 offset:40960
	global_load_dwordx4 v[136:139], v196, s[6:7]
	s_waitcnt lgkmcnt(10)
	v_mfma_f32_16x16x32_bf16 v[76:79], v[168:171], v[116:119], v[76:79]
	v_exp_f32_e32 v65, v65
	v_mfma_f32_16x16x32_bf16 v[72:75], v[168:171], v[100:103], v[72:75]
	v_exp_f32_e32 v69, v69
	ds_read_b128 v[164:167], v210 offset:16384
	global_load_dwordx4 v[140:143], v197, s[6:7]
	s_waitcnt lgkmcnt(9)
	v_mfma_f32_16x16x32_bf16 v[44:47], v[172:175], v[238:241], v[44:47]
	v_exp_f32_e32 v66, v66
	v_mfma_f32_16x16x32_bf16 v[40:43], v[172:175], v[216:219], v[40:43]
	v_exp_f32_e32 v70, v70
	ds_read_b128 v[168:171], v202 offset:40960
	s_waitcnt lgkmcnt(8)
	v_mfma_f32_16x16x32_bf16 v[72:75], v[176:179], v[104:107], v[72:75]
	v_exp_f32_e32 v67, v67
	v_mfma_f32_16x16x32_bf16 v[76:79], v[176:179], v[120:123], v[76:79]
	v_exp_f32_e32 v71, v71
	ds_read_b128 v[172:175], v210 offset:18432
	s_waitcnt lgkmcnt(7)
	v_mfma_f32_16x16x32_bf16 v[48:51], v[180:183], v[216:219], v[48:51]
	v_add_f32_e32 v220, v64, v65
	v_mfma_f32_16x16x32_bf16 v[52:55], v[180:183], v[238:241], v[52:55]
	v_add_f32_e32 v221, v68, v69
	ds_read_b128 v[176:179], v203 offset:40960
	s_waitcnt lgkmcnt(6)
	v_mfma_f32_16x16x32_bf16 v[76:79], v[230:233], v[124:127], v[76:79]
	v_add_f32_e32 v220, v220, v66
	v_mfma_f32_16x16x32_bf16 v[72:75], v[230:233], v[108:111], v[72:75]
	v_add_f32_e32 v221, v221, v70
	ds_read_b128 v[180:183], v210 offset:20480
	s_waitcnt lgkmcnt(6)
	v_mfma_f32_16x16x32_bf16 v[60:63], v[234:237], v[238:241], v[60:63]
	v_add_f32_e32 v220, v220, v67
	v_mfma_f32_16x16x32_bf16 v[56:59], v[234:237], v[216:219], v[56:59]
	v_add_f32_e32 v221, v221, v71
	ds_read_b128 v[230:233], v246 offset:40960
	s_waitcnt lgkmcnt(6)
	v_mfma_f32_16x16x32_bf16 v[80:83], v[160:163], v[96:99], 0
	v_exp_f32_e32 v72, v72
	v_exp_f32_e32 v76, v76
	v_mfma_f32_16x16x32_bf16 v[84:87], v[160:163], v[112:115], 0
	v_exp_f32_e32 v73, v73
	v_exp_f32_e32 v77, v77
	ds_read_b128 v[234:237], v210 offset:22528
	s_waitcnt lgkmcnt(6)
	v_mfma_f32_16x16x32_bf16 v[0:3], v[164:167], v[242:245], v[0:3]
	v_exp_f32_e32 v74, v74
	v_exp_f32_e32 v78, v78
	v_mfma_f32_16x16x32_bf16 v[4:7], v[164:167], v[204:207], v[4:7]
	v_exp_f32_e32 v75, v75
	v_exp_f32_e32 v79, v79
	ds_read_b128 v[160:163], v201 offset:45056
	s_waitcnt lgkmcnt(6)
	v_mfma_f32_16x16x32_bf16 v[84:87], v[168:171], v[116:119], v[84:87]
	v_add_f32_e32 v220, v220, v72
	v_mfma_f32_16x16x32_bf16 v[80:83], v[168:171], v[100:103], v[80:83]
	v_add_f32_e32 v221, v221, v76
	ds_read_b128 v[164:167], v210 offset:24576
	s_waitcnt lgkmcnt(6)
	v_mfma_f32_16x16x32_bf16 v[12:15], v[172:175], v[204:207], v[12:15]
	v_add_f32_e32 v220, v220, v73
	v_mfma_f32_16x16x32_bf16 v[8:11], v[172:175], v[242:245], v[8:11]
	v_add_f32_e32 v221, v221, v77
	ds_read_b128 v[168:171], v202 offset:45056
	s_waitcnt lgkmcnt(6)
	v_mfma_f32_16x16x32_bf16 v[80:83], v[176:179], v[104:107], v[80:83]
	v_add_f32_e32 v220, v220, v74
	v_mfma_f32_16x16x32_bf16 v[84:87], v[176:179], v[120:123], v[84:87]
	v_add_f32_e32 v221, v221, v78
	ds_read_b128 v[172:175], v210 offset:26624
	s_waitcnt lgkmcnt(6)
	v_mfma_f32_16x16x32_bf16 v[16:19], v[180:183], v[242:245], v[16:19]
	v_add_f32_e32 v220, v220, v75
	v_mfma_f32_16x16x32_bf16 v[20:23], v[180:183], v[204:207], v[20:23]
	v_add_f32_e32 v221, v221, v79
	ds_read_b128 v[176:179], v203 offset:45056
	s_waitcnt lgkmcnt(6)
	v_mfma_f32_16x16x32_bf16 v[84:87], v[230:233], v[124:127], v[84:87]
	v_cvt_pk_bf16_f32 v216, v64, v65
	v_mfma_f32_16x16x32_bf16 v[80:83], v[230:233], v[108:111], v[80:83]
	v_cvt_pk_bf16_f32 v217, v66, v67
	ds_read_b128 v[180:183], v210 offset:28672
	s_waitcnt lgkmcnt(6)
	v_mfma_f32_16x16x32_bf16 v[28:31], v[234:237], v[204:207], v[28:31]
	v_cvt_pk_bf16_f32 v238, v68, v69
	v_mfma_f32_16x16x32_bf16 v[24:27], v[234:237], v[242:245], v[24:27]
	v_cvt_pk_bf16_f32 v239, v70, v71
	ds_read_b128 v[230:233], v246 offset:45056
	s_waitcnt lgkmcnt(6)
	v_mfma_f32_16x16x32_bf16 v[88:91], v[160:163], v[96:99], 0
	v_exp_f32_e32 v80, v80
	v_exp_f32_e32 v84, v84
	v_mfma_f32_16x16x32_bf16 v[92:95], v[160:163], v[112:115], 0
	v_exp_f32_e32 v81, v81
	v_exp_f32_e32 v85, v85
	ds_read_b128 v[234:237], v210 offset:30720
	s_waitcnt lgkmcnt(6)
	v_mfma_f32_16x16x32_bf16 v[32:35], v[164:167], v[242:245], v[32:35]
	v_exp_f32_e32 v82, v82
	v_exp_f32_e32 v86, v86
	v_mfma_f32_16x16x32_bf16 v[36:39], v[164:167], v[204:207], v[36:39]
	v_exp_f32_e32 v83, v83
	v_exp_f32_e32 v87, v87
	s_waitcnt lgkmcnt(5)
	v_mfma_f32_16x16x32_bf16 v[92:95], v[168:171], v[116:119], v[92:95]
	v_add_f32_e32 v220, v220, v80
	v_mfma_f32_16x16x32_bf16 v[88:91], v[168:171], v[100:103], v[88:91]
	v_add_f32_e32 v221, v221, v84
	s_waitcnt lgkmcnt(4)
	v_mfma_f32_16x16x32_bf16 v[44:47], v[172:175], v[204:207], v[44:47]
	v_add_f32_e32 v220, v220, v81
	v_mfma_f32_16x16x32_bf16 v[40:43], v[172:175], v[242:245], v[40:43]
	v_add_f32_e32 v221, v221, v85
	s_waitcnt lgkmcnt(3)
	v_mfma_f32_16x16x32_bf16 v[88:91], v[176:179], v[104:107], v[88:91]
	v_add_f32_e32 v220, v220, v82
	v_mfma_f32_16x16x32_bf16 v[92:95], v[176:179], v[120:123], v[92:95]
	v_add_f32_e32 v221, v221, v86
	s_waitcnt lgkmcnt(0)
	s_barrier
	ds_read_b128 v[160:163], v201 offset:49152
	ds_read_b128 v[164:167], v209 offset:32768
	ds_read_b128 v[168:171], v202 offset:49152
	ds_read_b128 v[172:175], v209 offset:34816
	v_mfma_f32_16x16x32_bf16 v[48:51], v[180:183], v[242:245], v[48:51]
	v_add_f32_e32 v220, v220, v83
	v_mfma_f32_16x16x32_bf16 v[52:55], v[180:183], v[204:207], v[52:55]
	v_add_f32_e32 v221, v221, v87
	ds_read_b128 v[176:179], v203 offset:49152
	v_mfma_f32_16x16x32_bf16 v[92:95], v[230:233], v[124:127], v[92:95]
	v_cvt_pk_bf16_f32 v218, v72, v73
	v_mfma_f32_16x16x32_bf16 v[88:91], v[230:233], v[108:111], v[88:91]
	v_cvt_pk_bf16_f32 v219, v74, v75
	ds_read_b128 v[180:183], v209 offset:36864
	v_mfma_f32_16x16x32_bf16 v[60:63], v[234:237], v[204:207], v[60:63]
	v_cvt_pk_bf16_f32 v240, v76, v77
	v_mfma_f32_16x16x32_bf16 v[56:59], v[234:237], v[242:245], v[56:59]
	v_cvt_pk_bf16_f32 v241, v78, v79
	ds_read_b128 v[230:233], v246 offset:49152
	s_waitcnt lgkmcnt(6)
	v_mfma_f32_16x16x32_bf16 v[64:67], v[160:163], v[96:99], 0
	v_exp_f32_e32 v88, v88
	v_exp_f32_e32 v92, v92
	v_mfma_f32_16x16x32_bf16 v[68:71], v[160:163], v[112:115], 0
	v_cvt_pk_bf16_f32 v242, v80, v81
	v_exp_f32_e32 v89, v89
	ds_read_b128 v[234:237], v209 offset:38912
	s_add_u32 s8, s16, 0x3bc00300
	s_addc_u32 s9, s17, 0
	s_add_u32 s6, s15, 0x23a70000
	s_addc_u32 s7, s14, 0
	s_waitcnt lgkmcnt(6)
	v_mfma_f32_16x16x32_bf16 v[0:3], v[164:167], v[216:219], v[0:3]
	v_exp_f32_e32 v93, v93
	v_cvt_pk_bf16_f32 v243, v82, v83
	v_mfma_f32_16x16x32_bf16 v[4:7], v[164:167], v[238:241], v[4:7]
	v_exp_f32_e32 v90, v90
	v_exp_f32_e32 v94, v94
	ds_read_b128 v[160:163], v201 offset:53248
	s_waitcnt vmcnt(4)
	ds_write_b128 v225, v[152:155] offset:16384
	s_waitcnt lgkmcnt(7)
	v_mfma_f32_16x16x32_bf16 v[68:71], v[168:171], v[116:119], v[68:71]
	v_cvt_pk_bf16_f32 v204, v84, v85
	v_mfma_f32_16x16x32_bf16 v[64:67], v[168:171], v[100:103], v[64:67]
	v_exp_f32_e32 v91, v91
	ds_read_b128 v[164:167], v209 offset:40960
	ds_write_b128 v226, v[156:159] offset:16384
	s_waitcnt lgkmcnt(8)
	v_mfma_f32_16x16x32_bf16 v[12:15], v[172:175], v[238:241], v[12:15]
	v_exp_f32_e32 v95, v95
	v_mfma_f32_16x16x32_bf16 v[8:11], v[172:175], v[216:219], v[8:11]
	v_cvt_pk_bf16_f32 v205, v86, v87
	ds_read_b128 v[168:171], v202 offset:53248
	ds_write_b64 v227, v[132:133] offset:0
	s_waitcnt lgkmcnt(9)
	v_mfma_f32_16x16x32_bf16 v[64:67], v[176:179], v[104:107], v[64:67]
	v_add_f32_e32 v220, v220, v88
	v_mfma_f32_16x16x32_bf16 v[68:71], v[176:179], v[120:123], v[68:71]
	v_add_f32_e32 v221, v221, v92
	ds_read_b128 v[172:175], v209 offset:43008
	ds_write_b64 v228, v[134:135] offset:0
	s_waitcnt lgkmcnt(10)
	v_mfma_f32_16x16x32_bf16 v[16:19], v[180:183], v[216:219], v[16:19]
	v_add_f32_e32 v220, v220, v89
	v_mfma_f32_16x16x32_bf16 v[20:23], v[180:183], v[238:241], v[20:23]
	v_add_f32_e32 v221, v221, v93
	ds_read_b128 v[176:179], v203 offset:53248
	ds_write_b64 v229, v[128:129] offset:0
	s_waitcnt lgkmcnt(11)
	v_mfma_f32_16x16x32_bf16 v[68:71], v[230:233], v[124:127], v[68:71]
	v_cvt_pk_bf16_f32 v244, v88, v89
	v_mfma_f32_16x16x32_bf16 v[64:67], v[230:233], v[108:111], v[64:67]
	v_cvt_pk_bf16_f32 v245, v90, v91
	ds_read_b128 v[180:183], v209 offset:45056
	ds_write_b64 v184, v[130:131] offset:0
	s_waitcnt lgkmcnt(12)
	v_mfma_f32_16x16x32_bf16 v[28:31], v[234:237], v[238:241], v[28:31]
	v_cvt_pk_bf16_f32 v206, v92, v93
	v_mfma_f32_16x16x32_bf16 v[24:27], v[234:237], v[216:219], v[24:27]
	v_cvt_pk_bf16_f32 v207, v94, v95
	ds_read_b128 v[230:233], v246 offset:53248
	global_load_dwordx4 v[132:135], v198, s[8:9]
	s_waitcnt lgkmcnt(12)
	v_mfma_f32_16x16x32_bf16 v[72:75], v[160:163], v[96:99], 0
	v_add_f32_e32 v220, v220, v90
	v_add_f32_e32 v221, v221, v94
	v_mfma_f32_16x16x32_bf16 v[76:79], v[160:163], v[112:115], 0
	v_add_f32_e32 v220, v220, v91
	v_add_f32_e32 v221, v221, v95
	ds_read_b128 v[234:237], v209 offset:47104
	global_load_dwordx4 v[128:131], v199, s[8:9]
	s_waitcnt lgkmcnt(11)
	v_mfma_f32_16x16x32_bf16 v[32:35], v[164:167], v[216:219], v[32:35]
	v_add_f32_e32 v194, v194, v220
	v_add_f32_e32 v195, v195, v221
	v_mfma_f32_16x16x32_bf16 v[36:39], v[164:167], v[238:241], v[36:39]
	v_exp_f32_e32 v64, v64
	v_exp_f32_e32 v68, v68
	ds_read_b128 v[160:163], v201 offset:57344
	global_load_dwordx4 v[152:155], v196, s[6:7]
	s_waitcnt lgkmcnt(10)
	v_mfma_f32_16x16x32_bf16 v[76:79], v[168:171], v[116:119], v[76:79]
	v_exp_f32_e32 v65, v65
	v_mfma_f32_16x16x32_bf16 v[72:75], v[168:171], v[100:103], v[72:75]
	v_exp_f32_e32 v69, v69
	ds_read_b128 v[164:167], v210 offset:32768
	global_load_dwordx4 v[156:159], v197, s[6:7]
	s_waitcnt lgkmcnt(9)
	v_mfma_f32_16x16x32_bf16 v[44:47], v[172:175], v[238:241], v[44:47]
	v_exp_f32_e32 v66, v66
	v_mfma_f32_16x16x32_bf16 v[40:43], v[172:175], v[216:219], v[40:43]
	v_exp_f32_e32 v70, v70
	ds_read_b128 v[168:171], v202 offset:57344
	s_waitcnt lgkmcnt(8)
	v_mfma_f32_16x16x32_bf16 v[72:75], v[176:179], v[104:107], v[72:75]
	v_exp_f32_e32 v67, v67
	v_mfma_f32_16x16x32_bf16 v[76:79], v[176:179], v[120:123], v[76:79]
	v_exp_f32_e32 v71, v71
	ds_read_b128 v[172:175], v210 offset:34816
	s_waitcnt lgkmcnt(7)
	v_mfma_f32_16x16x32_bf16 v[48:51], v[180:183], v[216:219], v[48:51]
	v_add_f32_e32 v220, v64, v65
	v_mfma_f32_16x16x32_bf16 v[52:55], v[180:183], v[238:241], v[52:55]
	v_add_f32_e32 v221, v68, v69
	ds_read_b128 v[176:179], v203 offset:57344
	s_waitcnt lgkmcnt(6)
	v_mfma_f32_16x16x32_bf16 v[76:79], v[230:233], v[124:127], v[76:79]
	v_add_f32_e32 v220, v220, v66
	v_mfma_f32_16x16x32_bf16 v[72:75], v[230:233], v[108:111], v[72:75]
	v_add_f32_e32 v221, v221, v70
	ds_read_b128 v[180:183], v210 offset:36864
	s_waitcnt lgkmcnt(6)
	v_mfma_f32_16x16x32_bf16 v[60:63], v[234:237], v[238:241], v[60:63]
	v_add_f32_e32 v220, v220, v67
	v_mfma_f32_16x16x32_bf16 v[56:59], v[234:237], v[216:219], v[56:59]
	v_add_f32_e32 v221, v221, v71
	ds_read_b128 v[230:233], v246 offset:57344
	s_waitcnt lgkmcnt(6)
	v_mfma_f32_16x16x32_bf16 v[80:83], v[160:163], v[96:99], 0
	v_exp_f32_e32 v72, v72
	v_exp_f32_e32 v76, v76
	v_mfma_f32_16x16x32_bf16 v[84:87], v[160:163], v[112:115], 0
	v_exp_f32_e32 v73, v73
	v_exp_f32_e32 v77, v77
	ds_read_b128 v[234:237], v210 offset:38912
	s_waitcnt lgkmcnt(6)
	v_mfma_f32_16x16x32_bf16 v[0:3], v[164:167], v[242:245], v[0:3]
	v_exp_f32_e32 v74, v74
	v_exp_f32_e32 v78, v78
	v_mfma_f32_16x16x32_bf16 v[4:7], v[164:167], v[204:207], v[4:7]
	v_exp_f32_e32 v75, v75
	v_exp_f32_e32 v79, v79
	ds_read_b128 v[160:163], v201 offset:61440
	s_waitcnt lgkmcnt(6)
	v_mfma_f32_16x16x32_bf16 v[84:87], v[168:171], v[116:119], v[84:87]
	v_add_f32_e32 v220, v220, v72
	v_mfma_f32_16x16x32_bf16 v[80:83], v[168:171], v[100:103], v[80:83]
	v_add_f32_e32 v221, v221, v76
	ds_read_b128 v[164:167], v210 offset:40960
	s_waitcnt lgkmcnt(6)
	v_mfma_f32_16x16x32_bf16 v[12:15], v[172:175], v[204:207], v[12:15]
	v_add_f32_e32 v220, v220, v73
	v_mfma_f32_16x16x32_bf16 v[8:11], v[172:175], v[242:245], v[8:11]
	v_add_f32_e32 v221, v221, v77
	ds_read_b128 v[168:171], v202 offset:61440
	s_waitcnt lgkmcnt(6)
	v_mfma_f32_16x16x32_bf16 v[80:83], v[176:179], v[104:107], v[80:83]
	v_add_f32_e32 v220, v220, v74
	v_mfma_f32_16x16x32_bf16 v[84:87], v[176:179], v[120:123], v[84:87]
	v_add_f32_e32 v221, v221, v78
	ds_read_b128 v[172:175], v210 offset:43008
	s_waitcnt lgkmcnt(6)
	v_mfma_f32_16x16x32_bf16 v[16:19], v[180:183], v[242:245], v[16:19]
	v_add_f32_e32 v220, v220, v75
	v_mfma_f32_16x16x32_bf16 v[20:23], v[180:183], v[204:207], v[20:23]
	v_add_f32_e32 v221, v221, v79
	ds_read_b128 v[176:179], v203 offset:61440
	s_waitcnt lgkmcnt(6)
	v_mfma_f32_16x16x32_bf16 v[84:87], v[230:233], v[124:127], v[84:87]
	v_cvt_pk_bf16_f32 v216, v64, v65
	v_mfma_f32_16x16x32_bf16 v[80:83], v[230:233], v[108:111], v[80:83]
	v_cvt_pk_bf16_f32 v217, v66, v67
	ds_read_b128 v[180:183], v210 offset:45056
	s_waitcnt lgkmcnt(6)
	v_mfma_f32_16x16x32_bf16 v[28:31], v[234:237], v[204:207], v[28:31]
	v_cvt_pk_bf16_f32 v238, v68, v69
	v_mfma_f32_16x16x32_bf16 v[24:27], v[234:237], v[242:245], v[24:27]
	v_cvt_pk_bf16_f32 v239, v70, v71
	ds_read_b128 v[230:233], v246 offset:61440
	s_waitcnt lgkmcnt(6)
	v_mfma_f32_16x16x32_bf16 v[88:91], v[160:163], v[96:99], 0
	v_exp_f32_e32 v80, v80
	v_exp_f32_e32 v84, v84
	v_mfma_f32_16x16x32_bf16 v[92:95], v[160:163], v[112:115], 0
	v_exp_f32_e32 v81, v81
	v_exp_f32_e32 v85, v85
	ds_read_b128 v[234:237], v210 offset:47104
	s_waitcnt lgkmcnt(6)
	v_mfma_f32_16x16x32_bf16 v[32:35], v[164:167], v[242:245], v[32:35]
	v_exp_f32_e32 v82, v82
	v_exp_f32_e32 v86, v86
	v_mfma_f32_16x16x32_bf16 v[36:39], v[164:167], v[204:207], v[36:39]
	v_exp_f32_e32 v83, v83
	v_exp_f32_e32 v87, v87
	ds_read_b128 v[160:163], v201 offset:0
	s_waitcnt lgkmcnt(6)
	v_mfma_f32_16x16x32_bf16 v[92:95], v[168:171], v[116:119], v[92:95]
	v_add_f32_e32 v220, v220, v80
	v_mfma_f32_16x16x32_bf16 v[88:91], v[168:171], v[100:103], v[88:91]
	v_add_f32_e32 v221, v221, v84
	ds_read_b128 v[164:167], v209 offset:49152
	s_waitcnt lgkmcnt(6)
	v_mfma_f32_16x16x32_bf16 v[44:47], v[172:175], v[204:207], v[44:47]
	v_add_f32_e32 v220, v220, v81
	v_mfma_f32_16x16x32_bf16 v[40:43], v[172:175], v[242:245], v[40:43]
	v_add_f32_e32 v221, v221, v85
	ds_read_b128 v[168:171], v202 offset:0
	s_waitcnt lgkmcnt(6)
	v_mfma_f32_16x16x32_bf16 v[88:91], v[176:179], v[104:107], v[88:91]
	v_add_f32_e32 v220, v220, v82
	v_mfma_f32_16x16x32_bf16 v[92:95], v[176:179], v[120:123], v[92:95]
	v_add_f32_e32 v221, v221, v86
	ds_read_b128 v[172:175], v209 offset:51200
	s_waitcnt lgkmcnt(6)
	v_mfma_f32_16x16x32_bf16 v[48:51], v[180:183], v[242:245], v[48:51]
	v_add_f32_e32 v220, v220, v83
	v_mfma_f32_16x16x32_bf16 v[52:55], v[180:183], v[204:207], v[52:55]
	v_add_f32_e32 v221, v221, v87
	ds_read_b128 v[176:179], v203 offset:0
	s_waitcnt lgkmcnt(6)
	v_mfma_f32_16x16x32_bf16 v[92:95], v[230:233], v[124:127], v[92:95]
	v_cvt_pk_bf16_f32 v218, v72, v73
	v_mfma_f32_16x16x32_bf16 v[88:91], v[230:233], v[108:111], v[88:91]
	v_cvt_pk_bf16_f32 v219, v74, v75
	ds_read_b128 v[180:183], v209 offset:53248
	s_waitcnt lgkmcnt(6)
	v_mfma_f32_16x16x32_bf16 v[60:63], v[234:237], v[204:207], v[60:63]
	v_cvt_pk_bf16_f32 v240, v76, v77
	v_mfma_f32_16x16x32_bf16 v[56:59], v[234:237], v[242:245], v[56:59]
	v_cvt_pk_bf16_f32 v241, v78, v79
	ds_read_b128 v[230:233], v246 offset:0
	s_waitcnt lgkmcnt(6)
	v_mfma_f32_16x16x32_bf16 v[64:67], v[160:163], v[96:99], 0
	v_exp_f32_e32 v88, v88
	v_exp_f32_e32 v92, v92
	v_mfma_f32_16x16x32_bf16 v[68:71], v[160:163], v[112:115], 0
	v_cvt_pk_bf16_f32 v242, v80, v81
	v_exp_f32_e32 v89, v89
	ds_read_b128 v[234:237], v209 offset:55296
	s_add_u32 s8, s16, 0x3bc00380
	s_addc_u32 s9, s17, 0
	s_add_u32 s6, s15, 0x23a80000
	s_addc_u32 s7, s14, 0
	s_waitcnt lgkmcnt(6)
	v_mfma_f32_16x16x32_bf16 v[0:3], v[164:167], v[216:219], v[0:3]
	v_exp_f32_e32 v93, v93
	v_cvt_pk_bf16_f32 v243, v82, v83
	v_mfma_f32_16x16x32_bf16 v[4:7], v[164:167], v[238:241], v[4:7]
	v_exp_f32_e32 v90, v90
	v_exp_f32_e32 v94, v94
	ds_read_b128 v[160:163], v201 offset:4096
	s_waitcnt vmcnt(4)
	ds_write_b128 v225, v[136:139] offset:32768
	s_waitcnt lgkmcnt(7)
	v_mfma_f32_16x16x32_bf16 v[68:71], v[168:171], v[116:119], v[68:71]
	v_cvt_pk_bf16_f32 v204, v84, v85
	v_mfma_f32_16x16x32_bf16 v[64:67], v[168:171], v[100:103], v[64:67]
	v_exp_f32_e32 v91, v91
	ds_read_b128 v[164:167], v209 offset:57344
	ds_write_b128 v226, v[140:143] offset:32768
	s_waitcnt lgkmcnt(8)
	v_mfma_f32_16x16x32_bf16 v[12:15], v[172:175], v[238:241], v[12:15]
	v_exp_f32_e32 v95, v95
	v_mfma_f32_16x16x32_bf16 v[8:11], v[172:175], v[216:219], v[8:11]
	v_cvt_pk_bf16_f32 v205, v86, v87
	ds_read_b128 v[168:171], v202 offset:4096
	ds_write_b64 v227, v[148:149] offset:16384
	s_waitcnt lgkmcnt(9)
	v_mfma_f32_16x16x32_bf16 v[64:67], v[176:179], v[104:107], v[64:67]
	v_add_f32_e32 v220, v220, v88
	v_mfma_f32_16x16x32_bf16 v[68:71], v[176:179], v[120:123], v[68:71]
	v_add_f32_e32 v221, v221, v92
	ds_read_b128 v[172:175], v209 offset:59392
	ds_write_b64 v228, v[150:151] offset:16384
	s_waitcnt lgkmcnt(10)
	v_mfma_f32_16x16x32_bf16 v[16:19], v[180:183], v[216:219], v[16:19]
	v_add_f32_e32 v220, v220, v89
	v_mfma_f32_16x16x32_bf16 v[20:23], v[180:183], v[238:241], v[20:23]
	v_add_f32_e32 v221, v221, v93
	ds_read_b128 v[176:179], v203 offset:4096
	ds_write_b64 v229, v[144:145] offset:16384
	s_waitcnt lgkmcnt(11)
	v_mfma_f32_16x16x32_bf16 v[68:71], v[230:233], v[124:127], v[68:71]
	v_cvt_pk_bf16_f32 v244, v88, v89
	v_mfma_f32_16x16x32_bf16 v[64:67], v[230:233], v[108:111], v[64:67]
	v_cvt_pk_bf16_f32 v245, v90, v91
	ds_read_b128 v[180:183], v209 offset:61440
	ds_write_b64 v184, v[146:147] offset:16384
	s_waitcnt lgkmcnt(12)
	v_mfma_f32_16x16x32_bf16 v[28:31], v[234:237], v[238:241], v[28:31]
	v_cvt_pk_bf16_f32 v206, v92, v93
	v_mfma_f32_16x16x32_bf16 v[24:27], v[234:237], v[216:219], v[24:27]
	v_cvt_pk_bf16_f32 v207, v94, v95
	ds_read_b128 v[230:233], v246 offset:4096
	global_load_dwordx4 v[148:151], v198, s[8:9]
	s_waitcnt lgkmcnt(12)
	v_mfma_f32_16x16x32_bf16 v[72:75], v[160:163], v[96:99], 0
	v_add_f32_e32 v220, v220, v90
	v_add_f32_e32 v221, v221, v94
	v_mfma_f32_16x16x32_bf16 v[76:79], v[160:163], v[112:115], 0
	v_add_f32_e32 v220, v220, v91
	v_add_f32_e32 v221, v221, v95
	ds_read_b128 v[234:237], v209 offset:63488
	global_load_dwordx4 v[144:147], v199, s[8:9]
	s_waitcnt lgkmcnt(11)
	v_mfma_f32_16x16x32_bf16 v[32:35], v[164:167], v[216:219], v[32:35]
	v_add_f32_e32 v194, v194, v220
	v_add_f32_e32 v195, v195, v221
	v_mfma_f32_16x16x32_bf16 v[36:39], v[164:167], v[238:241], v[36:39]
	v_exp_f32_e32 v64, v64
	v_exp_f32_e32 v68, v68
	ds_read_b128 v[160:163], v201 offset:8192
	global_load_dwordx4 v[136:139], v196, s[6:7]
	s_waitcnt lgkmcnt(10)
	v_mfma_f32_16x16x32_bf16 v[76:79], v[168:171], v[116:119], v[76:79]
	v_exp_f32_e32 v65, v65
	v_mfma_f32_16x16x32_bf16 v[72:75], v[168:171], v[100:103], v[72:75]
	v_exp_f32_e32 v69, v69
	ds_read_b128 v[164:167], v210 offset:49152
	global_load_dwordx4 v[140:143], v197, s[6:7]
	s_waitcnt lgkmcnt(9)
	v_mfma_f32_16x16x32_bf16 v[44:47], v[172:175], v[238:241], v[44:47]
	v_exp_f32_e32 v66, v66
	v_mfma_f32_16x16x32_bf16 v[40:43], v[172:175], v[216:219], v[40:43]
	v_exp_f32_e32 v70, v70
	ds_read_b128 v[168:171], v202 offset:8192
	s_waitcnt lgkmcnt(8)
	v_mfma_f32_16x16x32_bf16 v[72:75], v[176:179], v[104:107], v[72:75]
	v_exp_f32_e32 v67, v67
	v_mfma_f32_16x16x32_bf16 v[76:79], v[176:179], v[120:123], v[76:79]
	v_exp_f32_e32 v71, v71
	ds_read_b128 v[172:175], v210 offset:51200
	s_waitcnt lgkmcnt(7)
	v_mfma_f32_16x16x32_bf16 v[48:51], v[180:183], v[216:219], v[48:51]
	v_add_f32_e32 v220, v64, v65
	v_mfma_f32_16x16x32_bf16 v[52:55], v[180:183], v[238:241], v[52:55]
	v_add_f32_e32 v221, v68, v69
	ds_read_b128 v[176:179], v203 offset:8192
	s_waitcnt lgkmcnt(6)
	v_mfma_f32_16x16x32_bf16 v[76:79], v[230:233], v[124:127], v[76:79]
	v_add_f32_e32 v220, v220, v66
	v_mfma_f32_16x16x32_bf16 v[72:75], v[230:233], v[108:111], v[72:75]
	v_add_f32_e32 v221, v221, v70
	ds_read_b128 v[180:183], v210 offset:53248
	s_waitcnt lgkmcnt(6)
	v_mfma_f32_16x16x32_bf16 v[60:63], v[234:237], v[238:241], v[60:63]
	v_add_f32_e32 v220, v220, v67
	v_mfma_f32_16x16x32_bf16 v[56:59], v[234:237], v[216:219], v[56:59]
	v_add_f32_e32 v221, v221, v71
	ds_read_b128 v[230:233], v246 offset:8192
	s_waitcnt lgkmcnt(6)
	v_mfma_f32_16x16x32_bf16 v[80:83], v[160:163], v[96:99], 0
	v_exp_f32_e32 v72, v72
	v_exp_f32_e32 v76, v76
	v_mfma_f32_16x16x32_bf16 v[84:87], v[160:163], v[112:115], 0
	v_exp_f32_e32 v73, v73
	v_exp_f32_e32 v77, v77
	ds_read_b128 v[234:237], v210 offset:55296
	s_waitcnt lgkmcnt(6)
	v_mfma_f32_16x16x32_bf16 v[0:3], v[164:167], v[242:245], v[0:3]
	v_exp_f32_e32 v74, v74
	v_exp_f32_e32 v78, v78
	v_mfma_f32_16x16x32_bf16 v[4:7], v[164:167], v[204:207], v[4:7]
	v_exp_f32_e32 v75, v75
	v_exp_f32_e32 v79, v79
	ds_read_b128 v[160:163], v201 offset:12288
	s_waitcnt lgkmcnt(6)
	v_mfma_f32_16x16x32_bf16 v[84:87], v[168:171], v[116:119], v[84:87]
	v_add_f32_e32 v220, v220, v72
	v_mfma_f32_16x16x32_bf16 v[80:83], v[168:171], v[100:103], v[80:83]
	v_add_f32_e32 v221, v221, v76
	ds_read_b128 v[164:167], v210 offset:57344
	s_waitcnt lgkmcnt(6)
	v_mfma_f32_16x16x32_bf16 v[12:15], v[172:175], v[204:207], v[12:15]
	v_add_f32_e32 v220, v220, v73
	v_mfma_f32_16x16x32_bf16 v[8:11], v[172:175], v[242:245], v[8:11]
	v_add_f32_e32 v221, v221, v77
	ds_read_b128 v[168:171], v202 offset:12288
	s_waitcnt lgkmcnt(6)
	v_mfma_f32_16x16x32_bf16 v[80:83], v[176:179], v[104:107], v[80:83]
	v_add_f32_e32 v220, v220, v74
	v_mfma_f32_16x16x32_bf16 v[84:87], v[176:179], v[120:123], v[84:87]
	v_add_f32_e32 v221, v221, v78
	ds_read_b128 v[172:175], v210 offset:59392
	s_add_u32 s10, s10, 0x200
	s_addc_u32 s11, s11, 0
	s_add_u32 s12, s12, 0x40000
	s_addc_u32 s13, s13, 0
	s_add_i32 s4, s4, 4
	s_cmpk_lt_u32 s4, 0x104
	s_cselect_b64 s[6:7], -1, 0
	s_and_b64 s[6:7], s[0:1], s[6:7]
	s_and_b64 vcc, exec, s[6:7]
	s_waitcnt lgkmcnt(6)
	v_mfma_f32_16x16x32_bf16 v[16:19], v[180:183], v[242:245], v[16:19]
	v_add_f32_e32 v220, v220, v75
	v_mfma_f32_16x16x32_bf16 v[20:23], v[180:183], v[204:207], v[20:23]
	v_add_f32_e32 v221, v221, v79
	ds_read_b128 v[176:179], v203 offset:12288
	s_waitcnt lgkmcnt(6)
	v_mfma_f32_16x16x32_bf16 v[84:87], v[230:233], v[124:127], v[84:87]
	v_cvt_pk_bf16_f32 v216, v64, v65
	v_mfma_f32_16x16x32_bf16 v[80:83], v[230:233], v[108:111], v[80:83]
	v_cvt_pk_bf16_f32 v217, v66, v67
	ds_read_b128 v[180:183], v210 offset:61440
	s_waitcnt lgkmcnt(6)
	v_mfma_f32_16x16x32_bf16 v[28:31], v[234:237], v[204:207], v[28:31]
	v_cvt_pk_bf16_f32 v238, v68, v69
	v_mfma_f32_16x16x32_bf16 v[24:27], v[234:237], v[242:245], v[24:27]
	v_cvt_pk_bf16_f32 v239, v70, v71
	ds_read_b128 v[230:233], v246 offset:12288
	s_waitcnt lgkmcnt(6)
	v_mfma_f32_16x16x32_bf16 v[88:91], v[160:163], v[96:99], 0
	v_exp_f32_e32 v80, v80
	v_exp_f32_e32 v84, v84
	v_mfma_f32_16x16x32_bf16 v[92:95], v[160:163], v[112:115], 0
	v_exp_f32_e32 v81, v81
	v_exp_f32_e32 v85, v85
	ds_read_b128 v[234:237], v210 offset:63488
	s_waitcnt lgkmcnt(6)
	v_mfma_f32_16x16x32_bf16 v[32:35], v[164:167], v[242:245], v[32:35]
	v_exp_f32_e32 v82, v82
	v_exp_f32_e32 v86, v86
	v_mfma_f32_16x16x32_bf16 v[36:39], v[164:167], v[204:207], v[36:39]
	v_exp_f32_e32 v83, v83
	v_exp_f32_e32 v87, v87
	s_waitcnt lgkmcnt(5)
	v_mfma_f32_16x16x32_bf16 v[92:95], v[168:171], v[116:119], v[92:95]
	v_add_f32_e32 v220, v220, v80
	v_mfma_f32_16x16x32_bf16 v[88:91], v[168:171], v[100:103], v[88:91]
	v_add_f32_e32 v221, v221, v84
	s_waitcnt lgkmcnt(4)
	v_mfma_f32_16x16x32_bf16 v[44:47], v[172:175], v[204:207], v[44:47]
	v_add_f32_e32 v220, v220, v81
	v_mfma_f32_16x16x32_bf16 v[40:43], v[172:175], v[242:245], v[40:43]
	v_add_f32_e32 v221, v221, v85
	s_waitcnt lgkmcnt(3)
	v_mfma_f32_16x16x32_bf16 v[88:91], v[176:179], v[104:107], v[88:91]
	v_add_f32_e32 v220, v220, v82
	v_mfma_f32_16x16x32_bf16 v[92:95], v[176:179], v[120:123], v[92:95]
	v_add_f32_e32 v221, v221, v86
	s_waitcnt lgkmcnt(0)
	s_barrier
	ds_read_b128 v[160:163], v201 offset:16384
	ds_read_b128 v[164:167], v209 offset:0
	ds_read_b128 v[168:171], v202 offset:16384
	ds_read_b128 v[172:175], v209 offset:2048
	v_mfma_f32_16x16x32_bf16 v[48:51], v[180:183], v[242:245], v[48:51]
	v_add_f32_e32 v220, v220, v83
	v_mfma_f32_16x16x32_bf16 v[52:55], v[180:183], v[204:207], v[52:55]
	v_add_f32_e32 v221, v221, v87
	ds_read_b128 v[176:179], v203 offset:16384
	v_mfma_f32_16x16x32_bf16 v[92:95], v[230:233], v[124:127], v[92:95]
	v_cvt_pk_bf16_f32 v218, v72, v73
	v_mfma_f32_16x16x32_bf16 v[88:91], v[230:233], v[108:111], v[88:91]
	v_cvt_pk_bf16_f32 v219, v74, v75
	ds_read_b128 v[180:183], v209 offset:4096
	v_mfma_f32_16x16x32_bf16 v[60:63], v[234:237], v[204:207], v[60:63]
	v_cvt_pk_bf16_f32 v240, v76, v77
	v_mfma_f32_16x16x32_bf16 v[56:59], v[234:237], v[242:245], v[56:59]
	v_cvt_pk_bf16_f32 v241, v78, v79
	ds_read_b128 v[230:233], v246 offset:16384
	s_cbranch_vccnz .LBB0_734
	s_waitcnt vmcnt(0)
	s_nop 7
	s_nop 7
	ds_swizzle_b32 v64, v194 offset:swizzle(SWAP,16)
	s_waitcnt lgkmcnt(0)
	v_add_f32_e32 v194, v194, v64
	v_mov_b32_e32 v65, v194
	s_nop 1
	v_permlane32_swap_b32_e32 v194, v65
	v_add_f32_e32 v194, v194, v65
	s_nop 0
	v_rcp_f32_e32 v66, v194
	ds_swizzle_b32 v64, v195 offset:swizzle(SWAP,16)
	s_waitcnt lgkmcnt(0)
	v_add_f32_e32 v195, v195, v64
	v_mov_b32_e32 v65, v195
	s_nop 1
	v_permlane32_swap_b32_e32 v195, v65
	v_add_f32_e32 v195, v195, v65
	s_nop 0
	v_rcp_f32_e32 v67, v195
	v_readlane_b32 s100, v250, 8
	v_mbcnt_lo_u32_b32 v68, -1, 0
	v_mbcnt_hi_u32_b32 v68, -1, v68
	v_and_b32_e32 v69, 15, v68
	v_lshrrev_b32_e32 v70, 4, v68
	s_lshr_b32 s101, s100, 1
	v_add_u32_e32 v69, s101, v69
	v_lshlrev_b32_e32 v69, 12, v69
	v_and_b32_e32 v71, 1, v70
	v_lshlrev_b32_e32 v71, 5, v71
	v_and_b32_e32 v70, 2, v70
	v_lshl_add_u32 v71, v70, 3, v71
	v_add_u32_e32 v70, v69, v71
	v_add_u32_e32 v71, 0x10000, v70
	v_mul_f32_e32 v0, v0, v66
	v_mul_f32_e32 v1, v1, v66
	v_mul_f32_e32 v2, v2, v66
	v_mul_f32_e32 v3, v3, v66
	v_mul_f32_e32 v8, v8, v66
	v_mul_f32_e32 v9, v9, v66
	v_mul_f32_e32 v10, v10, v66
	v_mul_f32_e32 v11, v11, v66
	v_cvt_pk_bf16_f32 v72, v0, v1
	v_cvt_pk_bf16_f32 v73, v2, v3
	v_cvt_pk_bf16_f32 v74, v8, v9
	v_cvt_pk_bf16_f32 v75, v10, v11
	s_nop 1
	v_permlane16_swap_b32_e32 v72, v74
	v_permlane16_swap_b32_e32 v73, v75
	s_nop 1
	global_store_dwordx4 v70, v[72:75], s[58:59] offset:0
	v_mul_f32_e32 v16, v16, v66
	v_mul_f32_e32 v17, v17, v66
	v_mul_f32_e32 v18, v18, v66
	v_mul_f32_e32 v19, v19, v66
	v_mul_f32_e32 v24, v24, v66
	v_mul_f32_e32 v25, v25, v66
	v_mul_f32_e32 v26, v26, v66
	v_mul_f32_e32 v27, v27, v66
	v_cvt_pk_bf16_f32 v76, v16, v17
	v_cvt_pk_bf16_f32 v77, v18, v19
	v_cvt_pk_bf16_f32 v78, v24, v25
	v_cvt_pk_bf16_f32 v79, v26, v27
	s_nop 1
	v_permlane16_swap_b32_e32 v76, v78
	v_permlane16_swap_b32_e32 v77, v79
	s_nop 1
	global_store_dwordx4 v70, v[76:79], s[58:59] offset:64
	v_mul_f32_e32 v32, v32, v66
	v_mul_f32_e32 v33, v33, v66
	v_mul_f32_e32 v34, v34, v66
	v_mul_f32_e32 v35, v35, v66
	v_mul_f32_e32 v40, v40, v66
	v_mul_f32_e32 v41, v41, v66
	v_mul_f32_e32 v42, v42, v66
	v_mul_f32_e32 v43, v43, v66
	v_cvt_pk_bf16_f32 v80, v32, v33
	v_cvt_pk_bf16_f32 v81, v34, v35
	v_cvt_pk_bf16_f32 v82, v40, v41
	v_cvt_pk_bf16_f32 v83, v42, v43
	s_nop 1
	v_permlane16_swap_b32_e32 v80, v82
	v_permlane16_swap_b32_e32 v81, v83
	s_nop 1
	global_store_dwordx4 v70, v[80:83], s[58:59] offset:128
	v_mul_f32_e32 v48, v48, v66
	v_mul_f32_e32 v49, v49, v66
	v_mul_f32_e32 v50, v50, v66
	v_mul_f32_e32 v51, v51, v66
	v_mul_f32_e32 v56, v56, v66
	v_mul_f32_e32 v57, v57, v66
	v_mul_f32_e32 v58, v58, v66
	v_mul_f32_e32 v59, v59, v66
	v_cvt_pk_bf16_f32 v84, v48, v49
	v_cvt_pk_bf16_f32 v85, v50, v51
	v_cvt_pk_bf16_f32 v86, v56, v57
	v_cvt_pk_bf16_f32 v87, v58, v59
	s_nop 1
	v_permlane16_swap_b32_e32 v84, v86
	v_permlane16_swap_b32_e32 v85, v87
	s_nop 1
	global_store_dwordx4 v70, v[84:87], s[58:59] offset:192
	v_mul_f32_e32 v4, v4, v67
	v_mul_f32_e32 v5, v5, v67
	v_mul_f32_e32 v6, v6, v67
	v_mul_f32_e32 v7, v7, v67
	v_mul_f32_e32 v12, v12, v67
	v_mul_f32_e32 v13, v13, v67
	v_mul_f32_e32 v14, v14, v67
	v_mul_f32_e32 v15, v15, v67
	v_cvt_pk_bf16_f32 v88, v4, v5
	v_cvt_pk_bf16_f32 v89, v6, v7
	v_cvt_pk_bf16_f32 v90, v12, v13
	v_cvt_pk_bf16_f32 v91, v14, v15
	s_nop 1
	v_permlane16_swap_b32_e32 v88, v90
	v_permlane16_swap_b32_e32 v89, v91
	s_nop 1
	global_store_dwordx4 v71, v[88:91], s[58:59] offset:0
	v_mul_f32_e32 v20, v20, v67
	v_mul_f32_e32 v21, v21, v67
	v_mul_f32_e32 v22, v22, v67
	v_mul_f32_e32 v23, v23, v67
	v_mul_f32_e32 v28, v28, v67
	v_mul_f32_e32 v29, v29, v67
	v_mul_f32_e32 v30, v30, v67
	v_mul_f32_e32 v31, v31, v67
	v_cvt_pk_bf16_f32 v92, v20, v21
	v_cvt_pk_bf16_f32 v93, v22, v23
	v_cvt_pk_bf16_f32 v94, v28, v29
	v_cvt_pk_bf16_f32 v95, v30, v31
	s_nop 1
	v_permlane16_swap_b32_e32 v92, v94
	v_permlane16_swap_b32_e32 v93, v95
	s_nop 1
	global_store_dwordx4 v71, v[92:95], s[58:59] offset:64
	v_mul_f32_e32 v36, v36, v67
	v_mul_f32_e32 v37, v37, v67
	v_mul_f32_e32 v38, v38, v67
	v_mul_f32_e32 v39, v39, v67
	v_mul_f32_e32 v44, v44, v67
	v_mul_f32_e32 v45, v45, v67
	v_mul_f32_e32 v46, v46, v67
	v_mul_f32_e32 v47, v47, v67
	v_cvt_pk_bf16_f32 v72, v36, v37
	v_cvt_pk_bf16_f32 v73, v38, v39
	v_cvt_pk_bf16_f32 v74, v44, v45
	v_cvt_pk_bf16_f32 v75, v46, v47
	s_nop 1
	v_permlane16_swap_b32_e32 v72, v74
	v_permlane16_swap_b32_e32 v73, v75
	s_nop 1
	global_store_dwordx4 v71, v[72:75], s[58:59] offset:128
	v_mul_f32_e32 v52, v52, v67
	v_mul_f32_e32 v53, v53, v67
	v_mul_f32_e32 v54, v54, v67
	v_mul_f32_e32 v55, v55, v67
	v_mul_f32_e32 v60, v60, v67
	v_mul_f32_e32 v61, v61, v67
	v_mul_f32_e32 v62, v62, v67
	v_mul_f32_e32 v63, v63, v67
	v_cvt_pk_bf16_f32 v76, v52, v53
	v_cvt_pk_bf16_f32 v77, v54, v55
	v_cvt_pk_bf16_f32 v78, v60, v61
	v_cvt_pk_bf16_f32 v79, v62, v63
	s_nop 1
	v_permlane16_swap_b32_e32 v76, v78
	v_permlane16_swap_b32_e32 v77, v79
	s_nop 1
	global_store_dwordx4 v71, v[76:79], s[58:59] offset:192
	s_barrier
